# v052 + diff K/V LDS-DMA in saddr form: scalar tile pointers, no 64-bit vector adds left in the attention loops
# baseline (speedup 1.0000x reference)
; __device__ __forceinline__ int kg(int row) { return (row >> 1) & 7; }
; __device__ __forceinline__ int v_rd_base(int lane) { return ((lane & 3) << 3) | (((lane >> 2) & 3) << 6) | (((lane >> 4) & 1) << 5) | (((lane >> 5) & 1) << 8); }
; #define BAR_ALL() asm volatile("s_waitcnt lgkmcnt(0)\n\ts_barrier" ::: "memory")
; #define DMA_K(tile, b) DMA_KP(Kh, tile, b)
; #define DMA_V(tile, b) DMA_VP(Vh, tile, b)
;     ...
;     float mhat = 0.f, l_reg = 0; bf16x8 qr[NQ];
; #pragma unroll
;     for (int d = 0; d < 4; ++d) o[d] = f32x16{};
;     const bf16_t* Qw = Qb + (long)((wid * QBLK + r32) * LDQ + hi * 8);
; #pragma unroll
;     for (int d0 = 0; d0 < NQ; ++d0) qr[d0] = *reinterpret_cast<const bf16x8*>(Qw + d0 * 16);
;     const int vb0 = (int)(uintptr_t)V_lds + v_rd_base(lane);
;     int ka[4];
; #pragma unroll
;     for (int b = 0; b < 4; ++b) ka[b] = (int)(uintptr_t)lds + r32 * RB + ((b * 32 + hi * 16) ^ (kg(r32) << 4));
;     f32x16 p0, p1; bf16x8 pa0, pa1, pa2, pa3;
;     asm volatile("s_waitcnt vmcnt(0)" ::: "memory"); BAR_ALL();
;     if (ATT_SKEW && g == 1) BAR_ALL();
;     ...
;     int ci = 0;
;     if (DMA_M) { DMA_K(2, 2); DMA_V(1, 1); }
;     SEG_M(true, false, 0, 0); BAR_ALL();
.LBB0_648:
	v_lshlrev_b32_e32 v26, 3, v156
	v_and_b32_e32 v23, 0xc0, v23
	s_cmp_lg_u32 0, -1
	v_and_or_b32 v23, v26, 24, v23
	v_and_b32_e32 v24, 32, v24
	v_and_b32_e32 v27, 0x100, v26
	s_cselect_b32 s10, 0, 0
	v_lshlrev_b32_e32 v154, 4, v25
	v_or3_b32 v23, v23, v24, v27
	v_lshl_add_u32 v24, v22, 7, s10
	v_and_b32_e32 v25, 0x70, v26
	v_add_u32_e32 v26, 32, v154
	v_xad_u32 v143, v26, v25, v24
	v_add_u32_e32 v26, 64, v154
	v_xad_u32 v160, v26, v25, v24
	v_add_u32_e32 v26, 0x60, v154
	v_xad_u32 v141, v154, v25, v24
	v_xad_u32 v161, v26, v25, v24
	s_addk_i32 s10, 0x6000
	ds_read_b128 v[24:27], v141 offset:0
	ds_read_b128 v[28:31], v141 offset:0x1000
	ds_read_b128 v[32:35], v143 offset:0
	ds_read_b128 v[36:39], v143 offset:0x1000
	v_add_u32_e32 v157, s10, v23
	v_cndmask_b32_e64 v23, 0, 1, s[26:27]
	s_mov_b32 s86, 0
	v_lshlrev_b32_e32 v23, 7, v23
	v_mov_b64_e32 v[94:95], v[14:15]
	v_mov_b64_e32 v[92:93], v[12:13]
	v_mov_b64_e32 v[90:91], v[10:11]
	v_mov_b64_e32 v[88:89], v[8:9]
	v_mov_b64_e32 v[86:87], v[6:7]
	v_mov_b64_e32 v[84:85], v[4:5]
	v_mov_b64_e32 v[82:83], v[2:3]
	v_mov_b64_e32 v[80:81], v[0:1]
	s_waitcnt lgkmcnt(3)
	s_waitcnt vmcnt(0)
	s_nop 0
	v_mfma_f32_32x32x16_bf16 v[96:111], v[24:27], v[112:115], v[80:95]
	ds_read_b128 v[24:27], v160 offset:0
	s_waitcnt lgkmcnt(3)
	s_nop 0
	v_mfma_f32_32x32x16_bf16 v[80:95], v[28:31], v[112:115], v[80:95]
	ds_read_b128 v[28:31], v160 offset:0x1000
	s_waitcnt lgkmcnt(3)
	s_nop 0
	v_mfma_f32_32x32x16_bf16 v[96:111], v[32:35], v[116:119], v[96:111]
	ds_read_b128 v[32:35], v161 offset:0
	s_waitcnt lgkmcnt(3)
	s_nop 0
	v_mfma_f32_32x32x16_bf16 v[80:95], v[36:39], v[116:119], v[80:95]
	ds_read_b128 v[36:39], v161 offset:0x1000
	s_waitcnt lgkmcnt(3)
	s_nop 0
	v_mfma_f32_32x32x16_bf16 v[96:111], v[24:27], v[120:123], v[96:111]
	s_waitcnt lgkmcnt(2)
	s_nop 0
	v_mfma_f32_32x32x16_bf16 v[80:95], v[28:31], v[120:123], v[80:95]
	s_waitcnt lgkmcnt(1)
	s_nop 0
	v_mfma_f32_32x32x16_bf16 v[96:111], v[32:35], v[124:127], v[96:111]
	s_waitcnt lgkmcnt(0)
	s_nop 0
	v_mfma_f32_32x32x16_bf16 v[80:95], v[36:39], v[124:127], v[80:95]
	s_and_b32 s46, s46, 3
	s_lshl_b64 s[44:45], s[44:45], 23
	s_lshl_b32 s46, s46, 8
	v_lshlrev_b32_e32 v20, 2, v20
	v_lshlrev_b32_e32 v17, 2, v17
	s_or_b32 s44, s44, s46
	v_and_b32_e32 v20, 0xffffe000, v20
	v_lshlrev_b32_e32 v18, 10, v18
	v_and_b32_e32 v17, 0xffffe000, v17
	v_lshl_add_u32 v155, v22, 2, s67
	v_or_b32_e32 v22, s44, v23
	v_mov_b32_e32 v23, s45
	v_or3_b32 v20, v20, v18, v21
	s_add_u32 s44, s73, s44
	v_or3_b32 v17, v17, v18, v19
	s_waitcnt lgkmcnt(0)
	s_barrier
	v_lshl_add_u64 v[22:23], s[24:25], 0, v[22:23]
	v_add_u32_e32 v20, v20, v16
	v_mov_b32_e32 v21, v139
	s_addc_u32 s45, s74, s45
	v_add_u32_e32 v16, v17, v16
	v_mov_b32_e32 v17, v139
	v_mov_b32_e32 v64, v139
	v_mov_b32_e32 v65, v139
	v_readfirstlane_b32 s98, v22
	v_readfirstlane_b32 s99, v23
	v_mov_b32_e32 v245, v20
	v_mov_b32_e32 v246, v16
	s_mov_b64 s[100:101], s[44:45]
	v_mov_b32_e32 v66, v139
	v_mov_b32_e32 v67, v139
	v_mov_b32_e32 v68, v139
	v_mov_b32_e32 v69, v139
	v_mov_b32_e32 v70, v139
	v_mov_b32_e32 v71, v139
	v_mov_b32_e32 v72, v139
	v_mov_b32_e32 v73, v139
	v_mov_b32_e32 v74, v139
	v_mov_b32_e32 v75, v139
	v_mov_b32_e32 v76, v139
	v_mov_b32_e32 v77, v139
	v_mov_b32_e32 v78, v139
	v_mov_b32_e32 v79, v139
	v_mov_b64_e32 v[48:49], v[64:65]
	v_mov_b64_e32 v[32:33], v[64:65]
	v_mov_b64_e32 v[16:17], v[64:65]
	v_cmp_gt_u32_e64 s[10:11], 32, v156
	v_mov_b32_e32 v159, 0
	s_mov_b64 s[44:45], 0
	v_mov_b64_e32 v[50:51], v[66:67]
	v_mov_b64_e32 v[52:53], v[68:69]
	v_mov_b64_e32 v[54:55], v[70:71]
	v_mov_b64_e32 v[56:57], v[72:73]
	v_mov_b64_e32 v[58:59], v[74:75]
	v_mov_b64_e32 v[60:61], v[76:77]
	v_mov_b64_e32 v[62:63], v[78:79]
	v_mov_b64_e32 v[34:35], v[66:67]
	v_mov_b64_e32 v[36:37], v[68:69]
	v_mov_b64_e32 v[38:39], v[70:71]
	v_mov_b64_e32 v[40:41], v[72:73]
	v_mov_b64_e32 v[42:43], v[74:75]
	v_mov_b64_e32 v[44:45], v[76:77]
	v_mov_b64_e32 v[46:47], v[78:79]
	v_mov_b64_e32 v[18:19], v[66:67]
	v_mov_b64_e32 v[20:21], v[68:69]
	v_mov_b64_e32 v[22:23], v[70:71]
	v_mov_b64_e32 v[24:25], v[72:73]
	v_mov_b64_e32 v[26:27], v[74:75]
	v_mov_b64_e32 v[28:29], v[76:77]
	v_mov_b64_e32 v[30:31], v[78:79]
	v_mov_b32_e32 v158, 0
	s_branch .LBB0_652

; #define PK4(P, BASE, OUT) do { u32x4 w = {cvtpk(P[BASE + 0], P[BASE + 1]), cvtpk(P[BASE + 2], P[BASE + 3]), cvtpk(P[BASE + 4], P[BASE + 5]), cvtpk(P[BASE + 6], P[BASE + 7])}; \
;     OUT = *reinterpret_cast<bf16x8*>(&w); } while (0)
; __device__ __forceinline__ void smax_tile(f32x16& p0, f32x16& p1, float& mhat, float& l_reg, f32x16 (&o)[4], float* al_l, const bool first, int r32, int hi,
;                                           bf16x8& pa0, bf16x8& pa1, bf16x8& pa2, bf16x8& pa3) {
;     ...
; #pragma unroll
;     for (int r = 0; r < 16; ++r) p0[r] = __builtin_amdgcn_exp2f(p0[r]);
; #pragma unroll
;     for (int r = 0; r < 16; ++r) p1[r] = __builtin_amdgcn_exp2f(p1[r]);
;     float ps = p0[0];
; #pragma unroll
;     for (int r = 1; r < 16; ++r) ps += p0[r];
; #pragma unroll
;     for (int r = 0; r < 16; ++r) ps += p1[r];
;     { auto rr = __builtin_amdgcn_permlane32_swap(__float_as_uint(ps), __float_as_uint(ps), false, false); ps = __uint_as_float(rr[0]) + __uint_as_float(rr[1]); }
;     l_reg += ps;
;     ...
;     PK4(p0, 0, pa0); PK4(p0, 8, pa1); PK4(p1, 0, pa2); PK4(p1, 8, pa3);
.LBB0_651:
	v_exp_f32_e32 v96, v96
	v_exp_f32_e32 v97, v97
	v_exp_f32_e32 v98, v98
	v_exp_f32_e32 v99, v99
	v_exp_f32_e32 v100, v100
	v_exp_f32_e32 v101, v101
	v_add_f32_e32 v128, v96, v97
	v_exp_f32_e32 v102, v102
	v_add_f32_e32 v128, v98, v128
	v_exp_f32_e32 v103, v103
	v_add_f32_e32 v128, v99, v128
	v_exp_f32_e32 v104, v104
	v_add_f32_e32 v128, v100, v128
	v_exp_f32_e32 v105, v105
	v_add_f32_e32 v128, v101, v128
	v_exp_f32_e32 v106, v106
	v_add_f32_e32 v128, v102, v128
	v_exp_f32_e32 v107, v107
	v_add_f32_e32 v128, v103, v128
	v_exp_f32_e32 v108, v108
	v_add_f32_e32 v128, v104, v128
	v_exp_f32_e32 v109, v109
	v_add_f32_e32 v128, v105, v128
	v_exp_f32_e32 v110, v110
	v_add_f32_e32 v128, v106, v128
	v_exp_f32_e32 v111, v111
	v_add_f32_e32 v128, v107, v128
	v_exp_f32_e32 v80, v80
	v_add_f32_e32 v128, v108, v128
	v_exp_f32_e32 v81, v81
	v_add_f32_e32 v128, v109, v128
	v_exp_f32_e32 v82, v82
	v_add_f32_e32 v128, v110, v128
	v_exp_f32_e32 v83, v83
	v_add_f32_e32 v128, v111, v128
	v_exp_f32_e32 v84, v84
	v_add_f32_e32 v128, v80, v128
	v_exp_f32_e32 v85, v85
	v_add_f32_e32 v128, v81, v128
	v_exp_f32_e32 v86, v86
	v_add_f32_e32 v128, v82, v128
	v_exp_f32_e32 v87, v87
	v_add_f32_e32 v128, v83, v128
	v_exp_f32_e32 v88, v88
	v_add_f32_e32 v128, v84, v128
	v_exp_f32_e32 v89, v89
	v_add_f32_e32 v128, v85, v128
	v_exp_f32_e32 v90, v90
	v_add_f32_e32 v128, v86, v128
	v_exp_f32_e32 v91, v91
	v_add_f32_e32 v128, v87, v128
	v_exp_f32_e32 v92, v92
	v_add_f32_e32 v128, v88, v128
	v_exp_f32_e32 v93, v93
	v_add_f32_e32 v128, v89, v128
	v_exp_f32_e32 v94, v94
	v_add_f32_e32 v128, v90, v128
	v_exp_f32_e32 v95, v95
	v_add_f32_e32 v128, v91, v128
	v_add_f32_e32 v128, v92, v128
	v_add_f32_e32 v128, v93, v128
	v_add_f32_e32 v128, v94, v128
	v_add_f32_e32 v128, v95, v128
	v_mov_b32_e32 v129, v128
	v_cvt_pk_bf16_f32 v162, v96, v97
	v_cvt_pk_bf16_f32 v163, v98, v99
	v_permlane32_swap_b32_e32 v128, v129
	v_add_f32_e32 v128, v128, v129
	v_add_f32_e32 v159, v159, v128
	v_cvt_pk_bf16_f32 v164, v100, v101
	v_cvt_pk_bf16_f32 v165, v102, v103
	v_cvt_pk_bf16_f32 v166, v104, v105
	v_cvt_pk_bf16_f32 v167, v106, v107
	v_cvt_pk_bf16_f32 v168, v108, v109
	v_cvt_pk_bf16_f32 v169, v110, v111
	v_cvt_pk_bf16_f32 v132, v80, v81
	v_cvt_pk_bf16_f32 v133, v82, v83
	v_cvt_pk_bf16_f32 v134, v84, v85
	v_cvt_pk_bf16_f32 v135, v86, v87
	v_cvt_pk_bf16_f32 v128, v88, v89
	v_cvt_pk_bf16_f32 v129, v90, v91
	v_cvt_pk_bf16_f32 v130, v92, v93
	v_cvt_pk_bf16_f32 v131, v94, v95
	s_cmp_lg_u32 s86, 0
	s_waitcnt lgkmcnt(0)
	s_barrier
; #define SBAR() __builtin_amdgcn_sched_barrier(0)
; #define DMA_K(tile, b) DMA_KP(Kh, tile, b)
; template <int DQK, bool HASQK, bool HASPV, int J>
; __device__ __forceinline__ void slot_read(bf16x8 (&kf)[DQK / 16][2], s16x4 (&vf)[4][8], const int (&ka_)[4], int vb_) {
;     constexpr int NQS = HASQK ? 2 * (DQK / 16) : 0, NS = NQS + (HASPV ? 16 : 0);
;     if constexpr (J < NQS) { constexpr int d0 = J >> 1, h = J & 1; dsr128<(d0 >> 2) * 128 + h * 32 * DQK * 2>(kf[d0][h], ka_[d0 & 3]); }
;     else if constexpr (J < NS) { constexpr int q = J - NQS, g = q >> 2, d = q & 3; dstr64<v_rd_off(d, g, 0)>(vf[g][2 * d], vb_); dstr64<v_rd_off(d, g, 1)>(vf[g][2 * d + 1], vb_); }
; }
; template <int DQK, bool HASQK, bool HASPV, int J> ...
;     constexpr int NQS = HASQK ? 2 * (DQK / 16) : 0, NS = NQS + (HASPV ? 16 : 0);
;     if constexpr (J < NS) {
;         constexpr int rd1 = (J + 1 < NS) ? ((J + 1 < NQS) ? 1 : 2) : 0, rd2 = (J + 2 < NS) ? ((J + 2 < NQS) ? 1 : 2) : 0, rd3 = (J + 3 < NS) ? ((J + 3 < NQS) ? 1 : 2) : 0, NW = rd1 + rd2 + rd3;
;     ...
;         if constexpr (J < NQS) { constexpr int d0 = J >> 1, h = J & 1;
;             LWN1(kf[d0][h]); SBAR();
;             if constexpr (h == 0) p0 = __builtin_amdgcn_mfma_f32_32x32x16_bf16(kf[d0][0], qr[d0], (d0 == 0) ? negm : p0, 0, 0, 0);
;             else p1 = __builtin_amdgcn_mfma_f32_32x32x16_bf16(kf[d0][1], qr[d0], (d0 == 0) ? negm : p1, 0, 0, 0);
;         } else { constexpr int q = J - NQS, g = q >> 2, d = q & 3;
;             LWN2(vf[g][2 * d], vf[g][2 * d + 1]); SBAR();
;             o[d] = __builtin_amdgcn_mfma_f32_32x32x16_bf16(pa[g], (bf16x8){vf[g][2 * d][0], vf[g][2 * d][1], vf[g][2 * d][2], vf[g][2 * d][3], vf[g][2 * d + 1][0], vf[g][2 * d + 1][1], vf[g][2 * d + 1][2], vf[g][2 * d + 1][3]}, o[d], 0, 0, 0);
;         }
;     ...
;         SBAR();
;         slot_read<DQK, HASQK, HASPV, J + 4>(kf, vf, ka_, vb_);
;         SBAR();
;         slot_run<DQK, HASQK, HASPV, J + 1>(kf, vf, ka_, vb_, qr, p0, p1, negm, o, pa);
;     }
; }
;     ...
;     int ci = 0;
;     if (DMA_M) { DMA_K(2, 2); DMA_V(1, 1); }
;     SEG_M(true, false, 0, 0); BAR_ALL();
; #pragma nounroll
;     for (int i = 0; i < NT - 1; ++i) {
;         SEG_S(i);
;         { const int cp = (ci == 0) ? 2 : ci - 1, cn = (ci == 2) ? 0 : ci + 1;
;           if (DMA_M) { if (i + 3 < NT) DMA_K(i + 3, cp); if (i + 2 < NT) DMA_V(i + 2, cn); }
;           SEG_M(true, true, ci, cp);
	s_cselect_b32 s46, s87, 0x8000
	s_lshl_b32 s47, s86, 13
	v_add_u32_e32 v81, s47, v141
	v_add_u32_e32 v82, s47, v143
	ds_read_b128 v[170:173], v81 offset:0
	ds_read_b128 v[174:177], v81 offset:0x1000
	ds_read_b128 v[178:181], v82 offset:0
	ds_read_b128 v[182:185], v82 offset:0x1000
	v_xor_b32_e32 v80, 0x80000000, v158
	v_add_u32_e32 v186, s47, v160
	v_add_u32_e32 v187, s47, v161
	v_add_u32_e32 v188, s46, v157
	v_mov_b32_e32 v81, v80
	v_mov_b32_e32 v82, v80
	v_mov_b32_e32 v83, v80
	v_mov_b32_e32 v84, v80
	v_mov_b32_e32 v85, v80
	v_mov_b32_e32 v86, v80
	v_mov_b32_e32 v87, v80
	v_mov_b32_e32 v88, v80
	v_mov_b32_e32 v89, v80
	v_mov_b32_e32 v90, v80
	v_mov_b32_e32 v91, v80
	v_mov_b32_e32 v92, v80
	v_mov_b32_e32 v93, v80
	v_mov_b32_e32 v94, v80
	v_mov_b32_e32 v95, v80
	s_waitcnt lgkmcnt(3)
	s_nop 1
	v_mfma_f32_32x32x16_bf16 v[96:111], v[170:173], v[112:115], v[80:95]
	ds_read_b128 v[170:173], v186 offset:0
	s_waitcnt lgkmcnt(3)
	s_nop 0
	v_mfma_f32_32x32x16_bf16 v[80:95], v[174:177], v[112:115], v[80:95]
	ds_read_b128 v[174:177], v186 offset:0x1000
	s_waitcnt lgkmcnt(3)
	s_nop 0
	v_mfma_f32_32x32x16_bf16 v[96:111], v[178:181], v[116:119], v[96:111]
	ds_read_b128 v[178:181], v187 offset:0
	s_waitcnt lgkmcnt(3)
	s_nop 0
	v_mfma_f32_32x32x16_bf16 v[80:95], v[182:185], v[116:119], v[80:95]
	ds_read_b128 v[182:185], v187 offset:0x1000
	s_waitcnt lgkmcnt(3)
	s_nop 0
	v_mfma_f32_32x32x16_bf16 v[96:111], v[170:173], v[120:123], v[96:111]
	ds_read_b64_tr_b16 v[170:171], v188 offset:0
	ds_read_b64_tr_b16 v[172:173], v188 offset:0x800
	s_waitcnt lgkmcnt(4)
	s_nop 0
	v_mfma_f32_32x32x16_bf16 v[80:95], v[174:177], v[120:123], v[80:95]
	ds_read_b64_tr_b16 v[174:175], v188 offset:0x200
	ds_read_b64_tr_b16 v[176:177], v188 offset:0xa00
	s_waitcnt lgkmcnt(5)
	s_nop 0
	v_mfma_f32_32x32x16_bf16 v[96:111], v[178:181], v[124:127], v[96:111]
	ds_read_b64_tr_b16 v[178:179], v188 offset:0x400
	ds_read_b64_tr_b16 v[180:181], v188 offset:0xc00
	s_waitcnt lgkmcnt(6)
	s_nop 0
	v_mfma_f32_32x32x16_bf16 v[80:95], v[182:185], v[124:127], v[80:95]
	ds_read_b64_tr_b16 v[182:183], v188 offset:0x600
	ds_read_b64_tr_b16 v[184:185], v188 offset:0xe00
	s_waitcnt lgkmcnt(6)
	s_nop 0
	v_mfma_f32_32x32x16_bf16 v[64:79], v[162:165], v[170:173], v[64:79]
	ds_read_b64_tr_b16 v[170:171], v188 offset:0x1000
	ds_read_b64_tr_b16 v[172:173], v188 offset:0x1800
	s_waitcnt lgkmcnt(6)
	s_nop 0
	v_mfma_f32_32x32x16_bf16 v[48:63], v[162:165], v[174:177], v[48:63]
	ds_read_b64_tr_b16 v[174:175], v188 offset:0x1200
	ds_read_b64_tr_b16 v[176:177], v188 offset:0x1a00
	s_waitcnt lgkmcnt(6)
	s_nop 0
	v_mfma_f32_32x32x16_bf16 v[32:47], v[162:165], v[178:181], v[32:47]
	ds_read_b64_tr_b16 v[178:179], v188 offset:0x1400
	ds_read_b64_tr_b16 v[180:181], v188 offset:0x1c00
	s_waitcnt lgkmcnt(6)
	s_nop 0
	v_mfma_f32_32x32x16_bf16 v[16:31], v[162:165], v[182:185], v[16:31]
	ds_read_b64_tr_b16 v[162:163], v188 offset:0x1600
	ds_read_b64_tr_b16 v[164:165], v188 offset:0x1e00
	s_waitcnt lgkmcnt(6)
	s_nop 0
	v_mfma_f32_32x32x16_bf16 v[64:79], v[166:169], v[170:173], v[64:79]
	ds_read_b64_tr_b16 v[170:171], v188 offset:0x2000
	ds_read_b64_tr_b16 v[172:173], v188 offset:0x2800
	s_waitcnt lgkmcnt(6)
	s_nop 0
	v_mfma_f32_32x32x16_bf16 v[48:63], v[166:169], v[174:177], v[48:63]
	ds_read_b64_tr_b16 v[174:175], v188 offset:0x2200
	ds_read_b64_tr_b16 v[176:177], v188 offset:0x2a00
	s_waitcnt lgkmcnt(6)
	s_nop 0
	v_mfma_f32_32x32x16_bf16 v[32:47], v[166:169], v[178:181], v[32:47]
	ds_read_b64_tr_b16 v[178:179], v188 offset:0x2400
	ds_read_b64_tr_b16 v[180:181], v188 offset:0x2c00
	s_waitcnt lgkmcnt(6)
	s_nop 0
	v_mfma_f32_32x32x16_bf16 v[16:31], v[166:169], v[162:165], v[16:31]
	ds_read_b64_tr_b16 v[162:163], v188 offset:0x2600
	ds_read_b64_tr_b16 v[164:165], v188 offset:0x2e00
	s_waitcnt lgkmcnt(6)
	s_nop 0
	v_mfma_f32_32x32x16_bf16 v[64:79], v[132:135], v[170:173], v[64:79]
	ds_read_b64_tr_b16 v[166:167], v188 offset:0x3000
	ds_read_b64_tr_b16 v[168:169], v188 offset:0x3800
	s_waitcnt lgkmcnt(6)
	s_nop 0
	v_mfma_f32_32x32x16_bf16 v[48:63], v[132:135], v[174:177], v[48:63]
	ds_read_b64_tr_b16 v[170:171], v188 offset:0x3200
	ds_read_b64_tr_b16 v[172:173], v188 offset:0x3a00
	s_waitcnt lgkmcnt(6)
	s_nop 0
	v_mfma_f32_32x32x16_bf16 v[32:47], v[132:135], v[178:181], v[32:47]
	ds_read_b64_tr_b16 v[174:175], v188 offset:0x3400
	ds_read_b64_tr_b16 v[176:177], v188 offset:0x3c00
	s_waitcnt lgkmcnt(6)
	s_nop 0
	v_mfma_f32_32x32x16_bf16 v[16:31], v[132:135], v[162:165], v[16:31]
	ds_read_b64_tr_b16 v[132:133], v188 offset:0x3600
	ds_read_b64_tr_b16 v[134:135], v188 offset:0x3e00
	s_waitcnt lgkmcnt(6)
	s_nop 0
	v_mfma_f32_32x32x16_bf16 v[64:79], v[128:131], v[166:169], v[64:79]
	s_waitcnt lgkmcnt(4)
	s_nop 0
	v_mfma_f32_32x32x16_bf16 v[48:63], v[128:131], v[170:173], v[48:63]
	s_waitcnt lgkmcnt(2)
	s_nop 0
	v_mfma_f32_32x32x16_bf16 v[32:47], v[128:131], v[174:177], v[32:47]
	s_waitcnt lgkmcnt(0)
	s_nop 0
	v_mfma_f32_32x32x16_bf16 v[16:31], v[128:131], v[132:135], v[16:31]
	s_add_u32 s98, s98, 0x10000
	s_addc_u32 s99, s99, 0
	s_add_u32 s100, s100, 0x10000
	s_addc_u32 s101, s101, 0
	s_waitcnt vmcnt(0)
	s_add_u32 s44, s44, 0x10000
	s_waitcnt lgkmcnt(0)
	s_barrier
	s_addc_u32 s45, s45, 0
	s_cmp_eq_u32 s44, 0x7f0000
	s_cbranch_scc1 .LBB0_662
.LBB0_652:
	s_cmp_eq_u32 s44, 0x7e0000
	s_cbranch_scc1 .LBB0_654
	s_lshl_b32 s46, s86, 13
	s_addk_i32 s46, 0xe000
	s_cmp_lg_u32 s86, 0
	s_cselect_b32 s46, s46, 0x4000
	s_add_i32 m0, s69, s46
	s_nop 0
	global_load_lds_dwordx4 v138, s[98:99]
.LBB0_654:
	s_add_i32 s46, s86, 1
	s_cmp_lg_u32 s86, 2
	s_cselect_b32 s86, s46, 0
	s_lshl_b32 s87, s86, 14
	s_add_i32 s46, s68, s87
	s_add_i32 m0, s46, 0x6000
	v_max3_f32 v128, v96, v97, v80
	global_load_lds_dwordx4 v245, s[100:101]
	s_add_i32 m0, s46, 0x6400
	v_max3_f32 v129, v98, v99, v81
	global_load_lds_dwordx4 v246, s[100:101]
	v_max3_f32 v128, v128, v82, v83
	v_max3_f32 v129, v129, v102, v103
	v_max3_f32 v128, v128, v100, v101
	v_max3_f32 v129, v129, v86, v87
	v_max3_f32 v128, v128, v84, v85
	v_max3_f32 v129, v129, v106, v107
	v_max3_f32 v128, v128, v104, v105
	v_max3_f32 v129, v129, v90, v91
	v_max3_f32 v128, v128, v88, v89
	v_max3_f32 v129, v129, v110, v111
	v_max3_f32 v128, v128, v108, v109
	v_max3_f32 v129, v129, v94, v95
	v_max3_f32 v128, v128, v92, v93
	v_max_f32 v128, v128, v129
	v_mov_b32_e32 v129, v128
	s_addk_i32 s87, 0xc000
	s_cmp_eq_u32 s44, 0
	v_permlane32_swap_b32_e32 v128, v129
	v_max_f32 v128, v128, v129
	s_cbranch_scc1 .LBB0_661
	v_cmp_lt_f32_e32 vcc, s79, v128
	s_cbranch_vccz .LBB0_651
	s_branch .LBB0_660
